# v52 + epilogue load de-serialisation: the post-norm gain vectors (4 x dwordx4) of the out-proj and down epilogues are requested before the row-statistics exchange wait instead of after it
# speedup vs baseline: 1.0033x; 1.0033x over previous
;     __device__ __forceinline__ void fused(f32x4 (&acc)[2][2][4][2], const Unit& u, int wr, int wc, int fr, int fq, PG8_LAS unsigned char* lds, int wid, int lane) const {
;     ...
;             for (int m = 0; m < 4; ++m) { const size_t off = (size_t)(u.pm * BM + ai * HALF + wr * 64 + m * 16 + fr) * DM + col0;
; #pragma unroll
;                 for (int bj = 0; bj < 2; ++bj) pre[ai][m][bj] = *(const u32x4*)(xr + off + bj * HALF); }
;         } else {
; #pragma unroll
;             for (int ai = 0; ai < 2; ++ai)
; #pragma unroll
;             for (int m = 0; m < 4; ++m)
; #pragma unroll
;                 for (int bj = 0; bj < 2; ++bj) pre[ai][m][bj] = (u32x4){0u, 0u, 0u, 0u};
;         }
;         (void)st1.finish(u, lds, wid, lane);
;     ...
;         if ((PROBE_KIND == 20 || PROBE_KIND == 21) && blockIdx.x == 0 && threadIdx.x == 0) atomicAdd((unsigned*)(wsb + WS_CTL) + 3010 + kind, (unsigned)(__builtin_amdgcn_s_memrealtime() - ts1_));
;     ...
;         f32x4 gv[2][2];
; #pragma unroll
;         for (int bj = 0; bj < 2; ++bj)
; #pragma unroll
;             for (int n = 0; n < 2; ++n) gv[bj][n] = *(const f32x4*)(g1 + col0 + bj * HALF + 4 * n);
.LBB0_1327:
	s_or_b64 exec, exec, s[10:11]
	s_lshl_b32 s8, s23, 5
	s_lshl_b32 s10, s16, 8
	v_lshrrev_b32_e32 v132, 1, v146
	s_or_b32 s8, s10, s8
	v_and_or_b32 v212, v132, 24, s8
	v_add_u32_e32 v132, s9, v215
	s_add_u32 s14, s12, 0x14000000
	v_or_b32_e32 v132, v132, v147
	s_addc_u32 s15, s13, 0
	v_ashrrev_i32_e32 v213, 31, v212
	v_ashrrev_i32_e32 v133, 31, v132
	v_lshl_add_u64 v[134:135], v[212:213], 1, s[14:15]
	v_lshlrev_b64 v[136:137], 11, v[132:133]
	v_lshl_add_u64 v[136:137], v[134:135], 0, v[136:137]
	global_load_dwordx4 v[208:211], v[136:137], off
	global_load_dwordx4 v[204:207], v[136:137], off offset:256
	v_or_b32_e32 v136, 16, v132
	v_ashrrev_i32_e32 v137, 31, v136
	v_lshlrev_b64 v[136:137], 11, v[136:137]
	v_lshl_add_u64 v[136:137], v[134:135], 0, v[136:137]
	global_load_dwordx4 v[200:203], v[136:137], off
	global_load_dwordx4 v[196:199], v[136:137], off offset:256
	v_or_b32_e32 v136, 32, v132
	v_ashrrev_i32_e32 v137, 31, v136
	v_lshlrev_b64 v[136:137], 11, v[136:137]
	v_lshl_add_u64 v[136:137], v[134:135], 0, v[136:137]
	global_load_dwordx4 v[192:195], v[136:137], off
	global_load_dwordx4 v[188:191], v[136:137], off offset:256
	v_or_b32_e32 v136, 48, v132
	v_ashrrev_i32_e32 v137, 31, v136
	v_lshlrev_b64 v[136:137], 11, v[136:137]
	v_lshl_add_u64 v[136:137], v[134:135], 0, v[136:137]
	global_load_dwordx4 v[184:187], v[136:137], off
	global_load_dwordx4 v[180:183], v[136:137], off offset:256
	v_add_u32_e32 v136, 0x80, v132
	v_ashrrev_i32_e32 v137, 31, v136
	v_lshlrev_b64 v[136:137], 11, v[136:137]
	v_lshl_add_u64 v[136:137], v[134:135], 0, v[136:137]
	global_load_dwordx4 v[176:179], v[136:137], off
	global_load_dwordx4 v[172:175], v[136:137], off offset:256
	v_add_u32_e32 v136, 0x90, v132
	v_ashrrev_i32_e32 v137, 31, v136
	v_lshlrev_b64 v[136:137], 11, v[136:137]
	v_lshl_add_u64 v[136:137], v[134:135], 0, v[136:137]
	global_load_dwordx4 v[168:171], v[136:137], off
	global_load_dwordx4 v[164:167], v[136:137], off offset:256
	v_add_u32_e32 v136, 0xa0, v132
	v_add_u32_e32 v132, 0xb0, v132
	v_ashrrev_i32_e32 v137, 31, v136
	v_ashrrev_i32_e32 v133, 31, v132
	v_lshlrev_b64 v[136:137], 11, v[136:137]
	v_lshlrev_b64 v[132:133], 11, v[132:133]
	v_lshl_add_u64 v[136:137], v[134:135], 0, v[136:137]
	v_lshl_add_u64 v[132:133], v[134:135], 0, v[132:133]
	global_load_dwordx4 v[160:163], v[136:137], off
	global_load_dwordx4 v[148:151], v[136:137], off offset:256
	s_nop 0
	global_load_dwordx4 v[136:139], v[132:133], off
	s_nop 0
	global_load_dwordx4 v[132:135], v[132:133], off offset:256
	s_memrealtime s[18:19]
	v_and_or_b32 v146, v146, 31, v216
	v_add_u32_e32 v140, v215, v146
	v_ashrrev_i32_e32 v141, 31, v140
	v_lshl_add_u64 v[144:145], v[140:141], 4, s[0:1]
	s_lshl_b32 s36, s77, 10
	s_lshl_b64 s[0:1], s[36:37], 2
	s_add_u32 s0, s12, s0
	s_addc_u32 s1, s13, s1
	v_lshl_add_u64 v[252:253], v[212:213], 2, s[0:1]
	s_mov_b64 s[0:1], 0x70c000
	v_lshl_add_u64 v[252:253], v[252:253], 0, s[0:1]
	global_load_dwordx4 v[236:239], v[252:253], off
	global_load_dwordx4 v[240:243], v[252:253], off offset:16
	global_load_dwordx4 v[244:247], v[252:253], off offset:512
	global_load_dwordx4 v[248:251], v[252:253], off offset:528
	s_branch .LBB0_1329

; __device__ __forceinline__ u32x4 pack8(const f32x4 a, const f32x4 b) { u32x4 w; w.x = cvt_pk_bf16(a[0], a[1]); w.y = cvt_pk_bf16(a[2], a[3]); w.z = cvt_pk_bf16(b[0], b[1]); w.w = cvt_pk_bf16(b[2], b[3]); return w; }
; __device__ __forceinline__ float bfl(unsigned w) { return __uint_as_float(w << 16); }
; __device__ __forceinline__ float bfh(unsigned w) { return __uint_as_float(w & 0xffff0000u); }
;     __device__ __forceinline__ void fused(f32x4 (&acc)[2][2][4][2], const Unit& u, int wr, int wc, int fr, int fq, PG8_LAS unsigned char* lds, int wid, int lane) const {
;     ...
;         f32x4 gv[2][2];
; #pragma unroll
;         for (int bj = 0; bj < 2; ++bj)
; #pragma unroll
;             for (int n = 0; n < 2; ++n) gv[bj][n] = *(const f32x4*)(g1 + col0 + bj * HALF + 4 * n);
; #pragma unroll
;         for (int ai = 0; ai < 2; ++ai)
; #pragma unroll
;             for (int m = 0; m < 4; ++m) { const int r = ai * HALF + wr * 64 + m * 16 + fr; const float sr = S[r]; const size_t off = (size_t)(u.pm * BM + r) * DM + col0; float ss = 0.f;
; #pragma unroll
;                 for (int bj = 0; bj < 2; ++bj) { f32x4 b0, b1;
;                     if (basef) { b0 = *(const f32x4*)(basef + off + bj * HALF); b1 = *(const f32x4*)(basef + off + bj * HALF + 4); }
;                     else { const u32x4 w = pre[ai][m][bj]; b0 = (f32x4){bfl(w.x), bfh(w.x), bfl(w.y), bfh(w.y)}; b1 = (f32x4){bfl(w.z), bfh(w.z), bfl(w.w), bfh(w.w)}; }
;                     const f32x4 x0 = b0 + acc[ai][bj][m][0] * sr * gv[bj][0], x1 = b1 + acc[ai][bj][m][1] * sr * gv[bj][1];
;                     if (outf) { __builtin_nontemporal_store(x0, (f32x4*)(outf + off + bj * HALF)); __builtin_nontemporal_store(x1, (f32x4*)(outf + off + bj * HALF + 4)); }
;                     else { *(u32x4*)(xr + off + bj * HALF) = pack8(x0, x1);
;                         ss += ((x0[0] * x0[0] + x0[1] * x0[1]) + (x0[2] * x0[2] + x0[3] * x0[3])) + ((x1[0] * x1[0] + x1[1] * x1[1]) + (x1[2] * x1[2] + x1[3] * x1[3])); } }
.LBB0_1339:
	s_or_b64 exec, exec, s[0:1]
	s_lshl_b32 s36, s77, 10
	s_lshl_b64 s[0:1], s[36:37], 2
	s_add_u32 s0, s12, s0
	s_addc_u32 s1, s13, s1
	v_lshl_add_u64 v[140:141], v[212:213], 2, s[0:1]
	s_mov_b64 s[0:1], 0x70c000
	v_lshl_add_u64 v[142:143], v[140:141], 0, s[0:1]
	s_mov_b32 s0, 0x70c000
	v_add_co_u32_e32 v140, vcc, s0, v140
	s_waitcnt lgkmcnt(0)
	s_barrier
	s_nop 0
	v_addc_co_u32_e32 v141, vcc, 0, v141, vcc
	v_mov_b32_e32 v152, v240
	v_mov_b32_e32 v153, v241
	v_mov_b32_e32 v154, v242
	v_mov_b32_e32 v155, v243
	v_mov_b32_e32 v144, v244
	v_mov_b32_e32 v145, v245
	v_mov_b32_e32 v146, v246
	v_mov_b32_e32 v147, v247
	v_mov_b32_e32 v156, v236
	v_mov_b32_e32 v157, v237
	v_mov_b32_e32 v158, v238
	v_mov_b32_e32 v159, v239
	s_nop 0
	v_mov_b32_e32 v140, v248
	v_mov_b32_e32 v141, v249
	v_mov_b32_e32 v142, v250
	v_mov_b32_e32 v143, v251
	v_lshl_add_u32 v217, v214, 2, 0
	ds_read_b32 v234, v217 offset:8192
	v_add_u32_e32 v218, v215, v214
	s_waitcnt vmcnt(0)
	v_lshlrev_b32_e32 v228, 16, v210
	v_and_b32_e32 v229, 0xffff0000, v210
	v_lshlrev_b32_e32 v210, 16, v211
	v_and_b32_e32 v211, 0xffff0000, v211
	s_waitcnt lgkmcnt(0)
	v_pk_mul_f32 v[124:125], v[124:125], v[234:235] op_sel_hi:[1,0]
	v_pk_mul_f32 v[126:127], v[126:127], v[234:235] op_sel_hi:[1,0]
	v_lshlrev_b32_e32 v220, 16, v208
	v_and_b32_e32 v221, 0xffff0000, v208
	v_lshlrev_b32_e32 v208, 16, v209
	v_and_b32_e32 v209, 0xffff0000, v209
	v_lshlrev_b32_e32 v230, 16, v204
	v_and_b32_e32 v231, 0xffff0000, v204
	v_lshlrev_b32_e32 v204, 16, v205
	v_and_b32_e32 v205, 0xffff0000, v205
	v_lshlrev_b32_e32 v232, 16, v206
	v_and_b32_e32 v233, 0xffff0000, v206
	v_lshlrev_b32_e32 v206, 16, v207
	v_and_b32_e32 v207, 0xffff0000, v207
	v_ashrrev_i32_e32 v219, 31, v218
	v_pk_mul_f32 v[130:131], v[130:131], v[234:235] op_sel_hi:[1,0]
	v_pk_mul_f32 v[128:129], v[128:129], v[234:235] op_sel_hi:[1,0]
	v_pk_mul_f32 v[120:121], v[120:121], v[234:235] op_sel_hi:[1,0]
	v_pk_mul_f32 v[122:123], v[122:123], v[234:235] op_sel_hi:[1,0]
	v_pk_mul_f32 v[116:117], v[116:117], v[234:235] op_sel_hi:[1,0]
	v_pk_mul_f32 v[118:119], v[118:119], v[234:235] op_sel_hi:[1,0]
	v_lshlrev_b64 v[218:219], 11, v[218:219]
	v_lshl_add_u64 v[218:219], s[14:15], 0, v[218:219]
	v_lshl_add_u64 v[218:219], v[212:213], 1, v[218:219]
	v_pk_fma_f32 v[126:127], v[154:155], v[126:127], v[210:211]
	v_pk_fma_f32 v[124:125], v[152:153], v[124:125], v[228:229]
	v_pk_fma_f32 v[122:123], v[146:147], v[122:123], v[204:205]
	v_pk_fma_f32 v[120:121], v[144:145], v[120:121], v[230:231]
	v_pk_fma_f32 v[128:129], v[156:157], v[128:129], v[220:221]
	v_pk_fma_f32 v[130:131], v[158:159], v[130:131], v[208:209]
	v_mul_f32_e32 v208, v125, v125
	v_mul_f32_e32 v209, v127, v127
	v_pk_fma_f32 v[204:205], v[142:143], v[118:119], v[206:207]
	v_pk_fma_f32 v[206:207], v[140:141], v[116:117], v[232:233]
	v_mul_f32_e32 v210, v121, v121
	v_mul_f32_e32 v211, v123, v123
	v_cvt_pk_bf16_f32 v116, v128, v129
	v_cvt_pk_bf16_f32 v117, v130, v131
	v_cvt_pk_bf16_f32 v118, v124, v125
	v_cvt_pk_bf16_f32 v119, v126, v127
	v_mul_f32_e32 v125, v129, v129
	v_mul_f32_e32 v127, v131, v131
	v_fmac_f32_e32 v208, v124, v124
	v_fmac_f32_e32 v209, v126, v126
	v_mul_f32_e32 v124, v207, v207
	v_mul_f32_e32 v126, v205, v205
	v_fmac_f32_e32 v210, v120, v120
	v_fmac_f32_e32 v211, v122, v122
	v_fmac_f32_e32 v125, v128, v128
	v_fmac_f32_e32 v127, v130, v130
	v_fmac_f32_e32 v124, v206, v206
	v_fmac_f32_e32 v126, v204, v204
	global_store_dwordx4 v[218:219], v[116:119], off
	s_nop 1
	v_add_f32_e32 v117, v208, v209
	v_cvt_pk_bf16_f32 v116, v120, v121
	v_add_f32_e32 v118, v210, v211
	v_add_f32_e32 v119, v125, v127
	v_add_f32_e32 v120, v124, v126
	v_add_f32_e32 v117, v119, v117
	v_add_f32_e32 v118, v118, v120
	v_add_f32_e32 v120, v117, v118
	ds_swizzle_b32 v121, v120 offset:swizzle(SWAP,16)
	v_cvt_pk_bf16_f32 v117, v122, v123
	v_cvt_pk_bf16_f32 v118, v206, v207
	v_cvt_pk_bf16_f32 v119, v204, v205
	global_store_dwordx4 v[218:219], v[116:119], off offset:256
	s_waitcnt lgkmcnt(0)
	s_nop 0
	v_add_f32_e32 v116, v120, v121
	v_mov_b32_e32 v117, v116
	s_nop 1
	v_permlane32_swap_b32_e32 v116, v117
	s_and_saveexec_b64 s[0:1], s[4:5]
	v_lshl_add_u32 v118, v214, 4, s20
	v_add_f32_e32 v116, v116, v117
	ds_write_b32 v118, v116
	s_or_b64 exec, exec, s[0:1]
	ds_read_b32 v118, v217 offset:8256
	v_or_b32_e32 v116, 16, v214
	v_add_u32_e32 v120, v215, v116
	v_ashrrev_i32_e32 v121, 31, v120
	v_lshlrev_b64 v[120:121], 11, v[120:121]
	v_lshl_add_u64 v[120:121], s[14:15], 0, v[120:121]
	v_lshlrev_b32_e32 v122, 16, v200
	v_and_b32_e32 v123, 0xffff0000, v200
	v_lshlrev_b32_e32 v124, 16, v201
	v_and_b32_e32 v125, 0xffff0000, v201
	v_lshlrev_b32_e32 v126, 16, v202
	v_and_b32_e32 v127, 0xffff0000, v202
	s_waitcnt lgkmcnt(0)
; __device__ __forceinline__ u32x4 pack8(const f32x4 a, const f32x4 b) { u32x4 w; w.x = cvt_pk_bf16(a[0], a[1]); w.y = cvt_pk_bf16(a[2], a[3]); w.z = cvt_pk_bf16(b[0], b[1]); w.w = cvt_pk_bf16(b[2], b[3]); return w; }
; __device__ __forceinline__ float bfl(unsigned w) { return __uint_as_float(w << 16); }
; __device__ __forceinline__ float bfh(unsigned w) { return __uint_as_float(w & 0xffff0000u); }
;     __device__ __forceinline__ void fused(f32x4 (&acc)[2][2][4][2], const Unit& u, int wr, int wc, int fr, int fq, PG8_LAS unsigned char* lds, int wid, int lane) const {
;     ...
;             for (int m = 0; m < 4; ++m) { const int r = ai * HALF + wr * 64 + m * 16 + fr; const float sr = S[r]; const size_t off = (size_t)(u.pm * BM + r) * DM + col0; float ss = 0.f;
; #pragma unroll
;                 for (int bj = 0; bj < 2; ++bj) { f32x4 b0, b1;
;                     if (basef) { b0 = *(const f32x4*)(basef + off + bj * HALF); b1 = *(const f32x4*)(basef + off + bj * HALF + 4); }
;                     else { const u32x4 w = pre[ai][m][bj]; b0 = (f32x4){bfl(w.x), bfh(w.x), bfl(w.y), bfh(w.y)}; b1 = (f32x4){bfl(w.z), bfh(w.z), bfl(w.w), bfh(w.w)}; }
;                     const f32x4 x0 = b0 + acc[ai][bj][m][0] * sr * gv[bj][0], x1 = b1 + acc[ai][bj][m][1] * sr * gv[bj][1];
;                     if (outf) { __builtin_nontemporal_store(x0, (f32x4*)(outf + off + bj * HALF)); __builtin_nontemporal_store(x1, (f32x4*)(outf + off + bj * HALF + 4)); }
;                     else { *(u32x4*)(xr + off + bj * HALF) = pack8(x0, x1);
;                         ss += ((x0[0] * x0[0] + x0[1] * x0[1]) + (x0[2] * x0[2] + x0[3] * x0[3])) + ((x1[0] * x1[0] + x1[1] * x1[1]) + (x1[2] * x1[2] + x1[3] * x1[3])); } }
;                 if (!outf) { ss = xor_add<16>(ss); ss = xor_add<32>(ss); if (fq == 0) P[r * 4 + wc] = ss; }
;                 if (m & 1) asm volatile("" ::: "memory"); }
	v_pk_mul_f32 v[112:113], v[112:113], v[118:119] op_sel_hi:[1,0]
	v_pk_mul_f32 v[114:115], v[114:115], v[118:119] op_sel_hi:[1,0]
	v_pk_mul_f32 v[108:109], v[108:109], v[118:119] op_sel_hi:[1,0]
	v_lshl_add_u64 v[120:121], v[212:213], 1, v[120:121]
	v_lshlrev_b32_e32 v128, 16, v203
	v_and_b32_e32 v129, 0xffff0000, v203
	v_pk_fma_f32 v[114:115], v[158:159], v[114:115], v[124:125]
	v_pk_fma_f32 v[112:113], v[156:157], v[112:113], v[122:123]
	v_pk_mul_f32 v[110:111], v[110:111], v[118:119] op_sel_hi:[1,0]
	v_pk_fma_f32 v[124:125], v[152:153], v[108:109], v[126:127]
	v_cvt_pk_bf16_f32 v108, v112, v113
	v_cvt_pk_bf16_f32 v109, v114, v115
	v_pk_fma_f32 v[122:123], v[154:155], v[110:111], v[128:129]
	v_cvt_pk_bf16_f32 v110, v124, v125
	v_pk_mul_f32 v[104:105], v[104:105], v[118:119] op_sel_hi:[1,0]
	v_cvt_pk_bf16_f32 v111, v122, v123
	global_store_dwordx4 v[120:121], v[108:111], off
	v_pk_mul_f32 v[106:107], v[106:107], v[118:119] op_sel_hi:[1,0]
	v_pk_mul_f32 v[100:101], v[100:101], v[118:119] op_sel_hi:[1,0]
	v_mul_f32_e32 v108, v113, v113
	v_mul_f32_e32 v109, v115, v115
	v_fmac_f32_e32 v108, v112, v112
	v_fmac_f32_e32 v109, v114, v114
	v_add_f32_e32 v108, v108, v109
	v_mul_f32_e32 v109, v125, v125
	v_mul_f32_e32 v110, v123, v123
	v_fmac_f32_e32 v109, v124, v124
	v_fmac_f32_e32 v110, v122, v122
	v_add_f32_e32 v109, v109, v110
	v_add_f32_e32 v117, v108, v109
	v_lshlrev_b32_e32 v108, 16, v196
	v_and_b32_e32 v109, 0xffff0000, v196
	v_lshlrev_b32_e32 v110, 16, v197
	v_and_b32_e32 v111, 0xffff0000, v197
	v_lshlrev_b32_e32 v112, 16, v198
	v_and_b32_e32 v113, 0xffff0000, v198
	v_lshlrev_b32_e32 v114, 16, v199
	v_and_b32_e32 v115, 0xffff0000, v199
	v_pk_fma_f32 v[104:105], v[144:145], v[104:105], v[108:109]
	v_pk_mul_f32 v[102:103], v[102:103], v[118:119] op_sel_hi:[1,0]
	v_pk_fma_f32 v[106:107], v[146:147], v[106:107], v[110:111]
	v_pk_fma_f32 v[108:109], v[142:143], v[102:103], v[114:115]
	v_pk_fma_f32 v[102:103], v[140:141], v[100:101], v[112:113]
	v_mul_f32_e32 v101, v105, v105
	v_cvt_pk_bf16_f32 v100, v104, v105
	v_fmac_f32_e32 v101, v104, v104
	v_mul_f32_e32 v104, v107, v107
	v_fmac_f32_e32 v104, v106, v106
	v_add_f32_e32 v101, v101, v104
	v_mul_f32_e32 v104, v103, v103
	v_mul_f32_e32 v105, v109, v109
	v_fmac_f32_e32 v104, v102, v102
	v_fmac_f32_e32 v105, v108, v108
	v_add_f32_e32 v104, v104, v105
	v_add_f32_e32 v101, v101, v104
	v_add_f32_e32 v104, v117, v101
	ds_swizzle_b32 v105, v104 offset:swizzle(SWAP,16)
	v_cvt_pk_bf16_f32 v101, v106, v107
	v_cvt_pk_bf16_f32 v102, v102, v103
	v_cvt_pk_bf16_f32 v103, v108, v109
	global_store_dwordx4 v[120:121], v[100:103], off offset:256
	s_waitcnt lgkmcnt(0)
	s_nop 0
	v_add_f32_e32 v100, v104, v105
	v_mov_b32_e32 v101, v100
	s_nop 1
	v_permlane32_swap_b32_e32 v100, v101
	s_and_saveexec_b64 s[0:1], s[4:5]
	v_lshl_add_u32 v102, v116, 4, s20
	v_add_f32_e32 v100, v100, v101
	ds_write_b32 v102, v100
	s_or_b64 exec, exec, s[0:1]
	ds_read_b32 v102, v217 offset:8320
	v_or_b32_e32 v100, 32, v214
	v_add_u32_e32 v104, v215, v100
	v_ashrrev_i32_e32 v105, 31, v104
	v_lshlrev_b64 v[104:105], 11, v[104:105]
	v_lshl_add_u64 v[104:105], s[14:15], 0, v[104:105]
	v_lshlrev_b32_e32 v106, 16, v192
	v_and_b32_e32 v107, 0xffff0000, v192
	v_lshlrev_b32_e32 v108, 16, v193
	v_and_b32_e32 v109, 0xffff0000, v193
	v_lshlrev_b32_e32 v110, 16, v194
	v_and_b32_e32 v111, 0xffff0000, v194
	s_waitcnt lgkmcnt(0)
	v_pk_mul_f32 v[96:97], v[96:97], v[102:103] op_sel_hi:[1,0]
	v_pk_mul_f32 v[98:99], v[98:99], v[102:103] op_sel_hi:[1,0]
	v_pk_mul_f32 v[92:93], v[92:93], v[102:103] op_sel_hi:[1,0]
	v_lshl_add_u64 v[104:105], v[212:213], 1, v[104:105]
	v_lshlrev_b32_e32 v112, 16, v195
	v_and_b32_e32 v113, 0xffff0000, v195
	v_pk_fma_f32 v[98:99], v[158:159], v[98:99], v[108:109]
	v_pk_fma_f32 v[96:97], v[156:157], v[96:97], v[106:107]
	v_pk_mul_f32 v[94:95], v[94:95], v[102:103] op_sel_hi:[1,0]
	v_pk_fma_f32 v[108:109], v[152:153], v[92:93], v[110:111]
	v_cvt_pk_bf16_f32 v92, v96, v97
	v_cvt_pk_bf16_f32 v93, v98, v99
	v_pk_fma_f32 v[106:107], v[154:155], v[94:95], v[112:113]
	v_cvt_pk_bf16_f32 v94, v108, v109
	v_pk_mul_f32 v[88:89], v[88:89], v[102:103] op_sel_hi:[1,0]
	v_cvt_pk_bf16_f32 v95, v106, v107
	global_store_dwordx4 v[104:105], v[92:95], off
	v_pk_mul_f32 v[90:91], v[90:91], v[102:103] op_sel_hi:[1,0]
	v_pk_mul_f32 v[84:85], v[84:85], v[102:103] op_sel_hi:[1,0]
	v_mul_f32_e32 v92, v97, v97
	v_mul_f32_e32 v93, v99, v99
	v_fmac_f32_e32 v92, v96, v96
	v_fmac_f32_e32 v93, v98, v98
	v_add_f32_e32 v92, v92, v93
	v_mul_f32_e32 v93, v109, v109
	v_mul_f32_e32 v94, v107, v107
	v_fmac_f32_e32 v93, v108, v108
	v_fmac_f32_e32 v94, v106, v106
	v_add_f32_e32 v93, v93, v94
	v_add_f32_e32 v101, v92, v93
	v_lshlrev_b32_e32 v92, 16, v188
	v_and_b32_e32 v93, 0xffff0000, v188
	v_lshlrev_b32_e32 v94, 16, v189
	v_and_b32_e32 v95, 0xffff0000, v189
	v_lshlrev_b32_e32 v96, 16, v190
	v_and_b32_e32 v97, 0xffff0000, v190
	v_lshlrev_b32_e32 v98, 16, v191
	v_and_b32_e32 v99, 0xffff0000, v191
	v_pk_fma_f32 v[88:89], v[144:145], v[88:89], v[92:93]
	v_pk_mul_f32 v[86:87], v[86:87], v[102:103] op_sel_hi:[1,0]
	v_pk_fma_f32 v[90:91], v[146:147], v[90:91], v[94:95]
	v_pk_fma_f32 v[92:93], v[142:143], v[86:87], v[98:99]
	v_pk_fma_f32 v[86:87], v[140:141], v[84:85], v[96:97]
	v_mul_f32_e32 v85, v89, v89
	v_cvt_pk_bf16_f32 v84, v88, v89
	v_fmac_f32_e32 v85, v88, v88
	v_mul_f32_e32 v88, v91, v91
	v_fmac_f32_e32 v88, v90, v90
	v_add_f32_e32 v85, v85, v88
	v_mul_f32_e32 v88, v87, v87
	v_mul_f32_e32 v89, v93, v93
	v_fmac_f32_e32 v88, v86, v86
	v_fmac_f32_e32 v89, v92, v92
	v_add_f32_e32 v88, v88, v89
	v_add_f32_e32 v85, v85, v88
	v_add_f32_e32 v88, v101, v85
	ds_swizzle_b32 v89, v88 offset:swizzle(SWAP,16)
	v_cvt_pk_bf16_f32 v85, v90, v91
	v_cvt_pk_bf16_f32 v86, v86, v87
	v_cvt_pk_bf16_f32 v87, v92, v93
	global_store_dwordx4 v[104:105], v[84:87], off offset:256
	s_waitcnt lgkmcnt(0)
; __device__ __forceinline__ u32x4 pack8(const f32x4 a, const f32x4 b) { u32x4 w; w.x = cvt_pk_bf16(a[0], a[1]); w.y = cvt_pk_bf16(a[2], a[3]); w.z = cvt_pk_bf16(b[0], b[1]); w.w = cvt_pk_bf16(b[2], b[3]); return w; }
; __device__ __forceinline__ float bfl(unsigned w) { return __uint_as_float(w << 16); }
; __device__ __forceinline__ float bfh(unsigned w) { return __uint_as_float(w & 0xffff0000u); }
;     __device__ __forceinline__ void fused(f32x4 (&acc)[2][2][4][2], const Unit& u, int wr, int wc, int fr, int fq, PG8_LAS unsigned char* lds, int wid, int lane) const {
;     ...
;             for (int m = 0; m < 4; ++m) { const int r = ai * HALF + wr * 64 + m * 16 + fr; const float sr = S[r]; const size_t off = (size_t)(u.pm * BM + r) * DM + col0; float ss = 0.f;
; #pragma unroll
;                 for (int bj = 0; bj < 2; ++bj) { f32x4 b0, b1;
;                     if (basef) { b0 = *(const f32x4*)(basef + off + bj * HALF); b1 = *(const f32x4*)(basef + off + bj * HALF + 4); }
;                     else { const u32x4 w = pre[ai][m][bj]; b0 = (f32x4){bfl(w.x), bfh(w.x), bfl(w.y), bfh(w.y)}; b1 = (f32x4){bfl(w.z), bfh(w.z), bfl(w.w), bfh(w.w)}; }
;                     const f32x4 x0 = b0 + acc[ai][bj][m][0] * sr * gv[bj][0], x1 = b1 + acc[ai][bj][m][1] * sr * gv[bj][1];
;                     if (outf) { __builtin_nontemporal_store(x0, (f32x4*)(outf + off + bj * HALF)); __builtin_nontemporal_store(x1, (f32x4*)(outf + off + bj * HALF + 4)); }
;                     else { *(u32x4*)(xr + off + bj * HALF) = pack8(x0, x1);
;                         ss += ((x0[0] * x0[0] + x0[1] * x0[1]) + (x0[2] * x0[2] + x0[3] * x0[3])) + ((x1[0] * x1[0] + x1[1] * x1[1]) + (x1[2] * x1[2] + x1[3] * x1[3])); } }
;                 if (!outf) { ss = xor_add<16>(ss); ss = xor_add<32>(ss); if (fq == 0) P[r * 4 + wc] = ss; }
;                 if (m & 1) asm volatile("" ::: "memory"); }
	s_nop 0
	v_add_f32_e32 v84, v88, v89
	v_mov_b32_e32 v85, v84
	s_nop 1
	v_permlane32_swap_b32_e32 v84, v85
	s_and_saveexec_b64 s[0:1], s[4:5]
	v_lshl_add_u32 v86, v100, 4, s20
	v_add_f32_e32 v84, v84, v85
	ds_write_b32 v86, v84
	s_or_b64 exec, exec, s[0:1]
	ds_read_b32 v86, v217 offset:8384
	v_or_b32_e32 v84, 48, v214
	v_add_u32_e32 v88, v215, v84
	v_ashrrev_i32_e32 v89, 31, v88
	v_lshlrev_b64 v[88:89], 11, v[88:89]
	v_lshl_add_u64 v[88:89], s[14:15], 0, v[88:89]
	v_lshlrev_b32_e32 v90, 16, v184
	v_and_b32_e32 v91, 0xffff0000, v184
	v_lshlrev_b32_e32 v92, 16, v185
	v_and_b32_e32 v93, 0xffff0000, v185
	v_lshlrev_b32_e32 v94, 16, v186
	v_and_b32_e32 v95, 0xffff0000, v186
	s_waitcnt lgkmcnt(0)
	v_pk_mul_f32 v[80:81], v[80:81], v[86:87] op_sel_hi:[1,0]
	v_pk_mul_f32 v[82:83], v[82:83], v[86:87] op_sel_hi:[1,0]
	v_pk_mul_f32 v[76:77], v[76:77], v[86:87] op_sel_hi:[1,0]
	v_lshl_add_u64 v[88:89], v[212:213], 1, v[88:89]
	v_lshlrev_b32_e32 v96, 16, v187
	v_and_b32_e32 v97, 0xffff0000, v187
	v_pk_fma_f32 v[82:83], v[158:159], v[82:83], v[92:93]
	v_pk_fma_f32 v[80:81], v[156:157], v[80:81], v[90:91]
	v_pk_mul_f32 v[78:79], v[78:79], v[86:87] op_sel_hi:[1,0]
	v_pk_fma_f32 v[92:93], v[152:153], v[76:77], v[94:95]
	v_cvt_pk_bf16_f32 v76, v80, v81
	v_cvt_pk_bf16_f32 v77, v82, v83
	v_pk_fma_f32 v[90:91], v[154:155], v[78:79], v[96:97]
	v_cvt_pk_bf16_f32 v78, v92, v93
	v_pk_mul_f32 v[72:73], v[72:73], v[86:87] op_sel_hi:[1,0]
	v_cvt_pk_bf16_f32 v79, v90, v91
	global_store_dwordx4 v[88:89], v[76:79], off
	v_pk_mul_f32 v[74:75], v[74:75], v[86:87] op_sel_hi:[1,0]
	v_pk_mul_f32 v[68:69], v[68:69], v[86:87] op_sel_hi:[1,0]
	v_mul_f32_e32 v76, v81, v81
	v_mul_f32_e32 v77, v83, v83
	v_fmac_f32_e32 v76, v80, v80
	v_fmac_f32_e32 v77, v82, v82
	v_add_f32_e32 v76, v76, v77
	v_mul_f32_e32 v77, v93, v93
	v_mul_f32_e32 v78, v91, v91
	v_fmac_f32_e32 v77, v92, v92
	v_fmac_f32_e32 v78, v90, v90
	v_add_f32_e32 v77, v77, v78
	v_add_f32_e32 v85, v76, v77
	v_lshlrev_b32_e32 v76, 16, v180
	v_and_b32_e32 v77, 0xffff0000, v180
	v_lshlrev_b32_e32 v78, 16, v181
	v_and_b32_e32 v79, 0xffff0000, v181
	v_lshlrev_b32_e32 v80, 16, v182
	v_and_b32_e32 v81, 0xffff0000, v182
	v_lshlrev_b32_e32 v82, 16, v183
	v_and_b32_e32 v83, 0xffff0000, v183
	v_pk_fma_f32 v[72:73], v[144:145], v[72:73], v[76:77]
	v_pk_mul_f32 v[70:71], v[70:71], v[86:87] op_sel_hi:[1,0]
	v_pk_fma_f32 v[74:75], v[146:147], v[74:75], v[78:79]
	v_pk_fma_f32 v[76:77], v[142:143], v[70:71], v[82:83]
	v_pk_fma_f32 v[70:71], v[140:141], v[68:69], v[80:81]
	v_mul_f32_e32 v69, v73, v73
	v_cvt_pk_bf16_f32 v68, v72, v73
	v_fmac_f32_e32 v69, v72, v72
	v_mul_f32_e32 v72, v75, v75
	v_fmac_f32_e32 v72, v74, v74
	v_add_f32_e32 v69, v69, v72
	v_mul_f32_e32 v72, v71, v71
	v_mul_f32_e32 v73, v77, v77
	v_fmac_f32_e32 v72, v70, v70
	v_fmac_f32_e32 v73, v76, v76
	v_add_f32_e32 v72, v72, v73
	v_add_f32_e32 v69, v69, v72
	v_add_f32_e32 v72, v85, v69
	ds_swizzle_b32 v73, v72 offset:swizzle(SWAP,16)
	v_cvt_pk_bf16_f32 v69, v74, v75
	v_cvt_pk_bf16_f32 v70, v70, v71
	v_cvt_pk_bf16_f32 v71, v76, v77
	global_store_dwordx4 v[88:89], v[68:71], off offset:256
	s_waitcnt lgkmcnt(0)
	s_nop 0
	v_add_f32_e32 v68, v72, v73
	v_mov_b32_e32 v69, v68
	s_nop 1
	v_permlane32_swap_b32_e32 v68, v69
	s_and_saveexec_b64 s[0:1], s[4:5]
	v_lshl_add_u32 v70, v84, 4, s20
	v_add_f32_e32 v68, v68, v69
	ds_write_b32 v70, v68
	s_or_b64 exec, exec, s[0:1]
	ds_read_b32 v70, v217 offset:8704
	v_add_u32_e32 v68, 0x80, v214
	v_add_u32_e32 v72, v215, v68
	v_ashrrev_i32_e32 v73, 31, v72
	v_lshlrev_b64 v[72:73], 11, v[72:73]
	v_lshl_add_u64 v[72:73], s[14:15], 0, v[72:73]
	v_lshlrev_b32_e32 v74, 16, v176
	v_and_b32_e32 v75, 0xffff0000, v176
	v_lshlrev_b32_e32 v76, 16, v177
	v_and_b32_e32 v77, 0xffff0000, v177
	v_lshlrev_b32_e32 v78, 16, v178
	v_and_b32_e32 v79, 0xffff0000, v178
	s_waitcnt lgkmcnt(0)
	v_pk_mul_f32 v[64:65], v[64:65], v[70:71] op_sel_hi:[1,0]
	v_pk_mul_f32 v[66:67], v[66:67], v[70:71] op_sel_hi:[1,0]
	v_pk_mul_f32 v[60:61], v[60:61], v[70:71] op_sel_hi:[1,0]
	v_lshl_add_u64 v[72:73], v[212:213], 1, v[72:73]
	v_lshlrev_b32_e32 v80, 16, v179
	v_and_b32_e32 v81, 0xffff0000, v179
	v_pk_fma_f32 v[66:67], v[158:159], v[66:67], v[76:77]
	v_pk_fma_f32 v[64:65], v[156:157], v[64:65], v[74:75]
	v_pk_mul_f32 v[62:63], v[62:63], v[70:71] op_sel_hi:[1,0]
	v_pk_fma_f32 v[76:77], v[152:153], v[60:61], v[78:79]
	v_cvt_pk_bf16_f32 v60, v64, v65
	v_cvt_pk_bf16_f32 v61, v66, v67
	v_pk_fma_f32 v[74:75], v[154:155], v[62:63], v[80:81]
	v_cvt_pk_bf16_f32 v62, v76, v77
	v_pk_mul_f32 v[56:57], v[56:57], v[70:71] op_sel_hi:[1,0]
	v_cvt_pk_bf16_f32 v63, v74, v75
	global_store_dwordx4 v[72:73], v[60:63], off
	v_pk_mul_f32 v[58:59], v[58:59], v[70:71] op_sel_hi:[1,0]
	v_pk_mul_f32 v[52:53], v[52:53], v[70:71] op_sel_hi:[1,0]
	v_mul_f32_e32 v60, v65, v65
	v_mul_f32_e32 v61, v67, v67
	v_fmac_f32_e32 v60, v64, v64
	v_fmac_f32_e32 v61, v66, v66
	v_add_f32_e32 v60, v60, v61
	v_mul_f32_e32 v61, v77, v77
	v_mul_f32_e32 v62, v75, v75
	v_fmac_f32_e32 v61, v76, v76
	v_fmac_f32_e32 v62, v74, v74
	v_add_f32_e32 v61, v61, v62
	v_add_f32_e32 v69, v60, v61
	v_lshlrev_b32_e32 v60, 16, v172
	v_and_b32_e32 v61, 0xffff0000, v172
	v_lshlrev_b32_e32 v62, 16, v173
	v_and_b32_e32 v63, 0xffff0000, v173
	v_lshlrev_b32_e32 v64, 16, v174
	v_and_b32_e32 v65, 0xffff0000, v174
	v_lshlrev_b32_e32 v66, 16, v175
	v_and_b32_e32 v67, 0xffff0000, v175
	v_pk_fma_f32 v[56:57], v[144:145], v[56:57], v[60:61]
	v_pk_mul_f32 v[54:55], v[54:55], v[70:71] op_sel_hi:[1,0]
	v_pk_fma_f32 v[58:59], v[146:147], v[58:59], v[62:63]
	v_pk_fma_f32 v[60:61], v[142:143], v[54:55], v[66:67]
	v_pk_fma_f32 v[54:55], v[140:141], v[52:53], v[64:65]
	v_mul_f32_e32 v53, v57, v57
	v_cvt_pk_bf16_f32 v52, v56, v57
	v_fmac_f32_e32 v53, v56, v56
	v_mul_f32_e32 v56, v59, v59
	v_fmac_f32_e32 v56, v58, v58
	v_add_f32_e32 v53, v53, v56
	v_mul_f32_e32 v56, v55, v55
	v_mul_f32_e32 v57, v61, v61
	v_fmac_f32_e32 v56, v54, v54
	v_fmac_f32_e32 v57, v60, v60
	v_add_f32_e32 v56, v56, v57
	v_add_f32_e32 v53, v53, v56
	v_add_f32_e32 v56, v69, v53
	ds_swizzle_b32 v57, v56 offset:swizzle(SWAP,16)
	v_cvt_pk_bf16_f32 v53, v58, v59
	v_cvt_pk_bf16_f32 v54, v54, v55
	v_cvt_pk_bf16_f32 v55, v60, v61
	global_store_dwordx4 v[72:73], v[52:55], off offset:256
	s_waitcnt lgkmcnt(0)
; __device__ __forceinline__ u32x4 pack8(const f32x4 a, const f32x4 b) { u32x4 w; w.x = cvt_pk_bf16(a[0], a[1]); w.y = cvt_pk_bf16(a[2], a[3]); w.z = cvt_pk_bf16(b[0], b[1]); w.w = cvt_pk_bf16(b[2], b[3]); return w; }
; __device__ __forceinline__ float bfl(unsigned w) { return __uint_as_float(w << 16); }
; __device__ __forceinline__ float bfh(unsigned w) { return __uint_as_float(w & 0xffff0000u); }
;     __device__ __forceinline__ void fused(f32x4 (&acc)[2][2][4][2], const Unit& u, int wr, int wc, int fr, int fq, PG8_LAS unsigned char* lds, int wid, int lane) const {
;     ...
;         for (int ai = 0; ai < 2; ++ai)
; #pragma unroll
;             for (int m = 0; m < 4; ++m) { const int r = ai * HALF + wr * 64 + m * 16 + fr; const float sr = S[r]; const size_t off = (size_t)(u.pm * BM + r) * DM + col0; float ss = 0.f;
; #pragma unroll
;                 for (int bj = 0; bj < 2; ++bj) { f32x4 b0, b1;
;                     if (basef) { b0 = *(const f32x4*)(basef + off + bj * HALF); b1 = *(const f32x4*)(basef + off + bj * HALF + 4); }
;                     else { const u32x4 w = pre[ai][m][bj]; b0 = (f32x4){bfl(w.x), bfh(w.x), bfl(w.y), bfh(w.y)}; b1 = (f32x4){bfl(w.z), bfh(w.z), bfl(w.w), bfh(w.w)}; }
;                     const f32x4 x0 = b0 + acc[ai][bj][m][0] * sr * gv[bj][0], x1 = b1 + acc[ai][bj][m][1] * sr * gv[bj][1];
;                     if (outf) { __builtin_nontemporal_store(x0, (f32x4*)(outf + off + bj * HALF)); __builtin_nontemporal_store(x1, (f32x4*)(outf + off + bj * HALF + 4)); }
;                     else { *(u32x4*)(xr + off + bj * HALF) = pack8(x0, x1);
;                         ss += ((x0[0] * x0[0] + x0[1] * x0[1]) + (x0[2] * x0[2] + x0[3] * x0[3])) + ((x1[0] * x1[0] + x1[1] * x1[1]) + (x1[2] * x1[2] + x1[3] * x1[3])); } }
;                 if (!outf) { ss = xor_add<16>(ss); ss = xor_add<32>(ss); if (fq == 0) P[r * 4 + wc] = ss; }
;                 if (m & 1) asm volatile("" ::: "memory"); }
	s_nop 0
	v_add_f32_e32 v52, v56, v57
	v_mov_b32_e32 v53, v52
	s_nop 1
	v_permlane32_swap_b32_e32 v52, v53
	s_and_saveexec_b64 s[0:1], s[4:5]
	v_lshl_add_u32 v54, v68, 4, s20
	v_add_f32_e32 v52, v52, v53
	ds_write_b32 v54, v52
	s_or_b64 exec, exec, s[0:1]
	ds_read_b32 v54, v217 offset:8768
	v_add_u32_e32 v52, 0x90, v214
	v_add_u32_e32 v56, v215, v52
	v_ashrrev_i32_e32 v57, 31, v56
	v_lshlrev_b64 v[56:57], 11, v[56:57]
	v_lshl_add_u64 v[56:57], s[14:15], 0, v[56:57]
	v_lshlrev_b32_e32 v58, 16, v168
	v_and_b32_e32 v59, 0xffff0000, v168
	v_lshlrev_b32_e32 v60, 16, v169
	v_and_b32_e32 v61, 0xffff0000, v169
	v_lshlrev_b32_e32 v62, 16, v170
	v_and_b32_e32 v63, 0xffff0000, v170
	s_waitcnt lgkmcnt(0)
	v_pk_mul_f32 v[48:49], v[48:49], v[54:55] op_sel_hi:[1,0]
	v_pk_mul_f32 v[50:51], v[50:51], v[54:55] op_sel_hi:[1,0]
	v_pk_mul_f32 v[44:45], v[44:45], v[54:55] op_sel_hi:[1,0]
	v_lshl_add_u64 v[56:57], v[212:213], 1, v[56:57]
	v_lshlrev_b32_e32 v64, 16, v171
	v_and_b32_e32 v65, 0xffff0000, v171
	v_pk_fma_f32 v[50:51], v[158:159], v[50:51], v[60:61]
	v_pk_fma_f32 v[48:49], v[156:157], v[48:49], v[58:59]
	v_pk_mul_f32 v[46:47], v[46:47], v[54:55] op_sel_hi:[1,0]
	v_pk_fma_f32 v[60:61], v[152:153], v[44:45], v[62:63]
	v_cvt_pk_bf16_f32 v44, v48, v49
	v_cvt_pk_bf16_f32 v45, v50, v51
	v_pk_fma_f32 v[58:59], v[154:155], v[46:47], v[64:65]
	v_cvt_pk_bf16_f32 v46, v60, v61
	v_pk_mul_f32 v[40:41], v[40:41], v[54:55] op_sel_hi:[1,0]
	v_cvt_pk_bf16_f32 v47, v58, v59
	global_store_dwordx4 v[56:57], v[44:47], off
	v_pk_mul_f32 v[42:43], v[42:43], v[54:55] op_sel_hi:[1,0]
	v_pk_mul_f32 v[36:37], v[36:37], v[54:55] op_sel_hi:[1,0]
	v_mul_f32_e32 v44, v49, v49
	v_mul_f32_e32 v45, v51, v51
	v_fmac_f32_e32 v44, v48, v48
	v_fmac_f32_e32 v45, v50, v50
	v_add_f32_e32 v44, v44, v45
	v_mul_f32_e32 v45, v61, v61
	v_mul_f32_e32 v46, v59, v59
	v_fmac_f32_e32 v45, v60, v60
	v_fmac_f32_e32 v46, v58, v58
	v_add_f32_e32 v45, v45, v46
	v_add_f32_e32 v53, v44, v45
	v_lshlrev_b32_e32 v44, 16, v164
	v_and_b32_e32 v45, 0xffff0000, v164
	v_lshlrev_b32_e32 v46, 16, v165
	v_and_b32_e32 v47, 0xffff0000, v165
	v_lshlrev_b32_e32 v48, 16, v166
	v_and_b32_e32 v49, 0xffff0000, v166
	v_lshlrev_b32_e32 v50, 16, v167
	v_and_b32_e32 v51, 0xffff0000, v167
	v_pk_fma_f32 v[40:41], v[144:145], v[40:41], v[44:45]
	v_pk_mul_f32 v[38:39], v[38:39], v[54:55] op_sel_hi:[1,0]
	v_pk_fma_f32 v[42:43], v[146:147], v[42:43], v[46:47]
	v_pk_fma_f32 v[44:45], v[142:143], v[38:39], v[50:51]
	v_pk_fma_f32 v[38:39], v[140:141], v[36:37], v[48:49]
	v_mul_f32_e32 v37, v41, v41
	v_cvt_pk_bf16_f32 v36, v40, v41
	v_fmac_f32_e32 v37, v40, v40
	v_mul_f32_e32 v40, v43, v43
	v_fmac_f32_e32 v40, v42, v42
	v_add_f32_e32 v37, v37, v40
	v_mul_f32_e32 v40, v39, v39
	v_mul_f32_e32 v41, v45, v45
	v_fmac_f32_e32 v40, v38, v38
	v_fmac_f32_e32 v41, v44, v44
	v_add_f32_e32 v40, v40, v41
	v_add_f32_e32 v37, v37, v40
	v_add_f32_e32 v40, v53, v37
	ds_swizzle_b32 v41, v40 offset:swizzle(SWAP,16)
	v_cvt_pk_bf16_f32 v37, v42, v43
	v_cvt_pk_bf16_f32 v38, v38, v39
	v_cvt_pk_bf16_f32 v39, v44, v45
	global_store_dwordx4 v[56:57], v[36:39], off offset:256
	s_waitcnt lgkmcnt(0)
	s_nop 0
	v_add_f32_e32 v36, v40, v41
	v_mov_b32_e32 v37, v36
	s_nop 1
	v_permlane32_swap_b32_e32 v36, v37
	s_and_saveexec_b64 s[0:1], s[4:5]
	v_lshl_add_u32 v38, v52, 4, s20
	v_add_f32_e32 v36, v36, v37
	ds_write_b32 v38, v36
	s_or_b64 exec, exec, s[0:1]
	ds_read_b32 v38, v217 offset:8832
	v_add_u32_e32 v36, 0xa0, v214
	v_add_u32_e32 v40, v215, v36
	v_ashrrev_i32_e32 v41, 31, v40
	v_lshlrev_b64 v[40:41], 11, v[40:41]
	v_lshl_add_u64 v[40:41], s[14:15], 0, v[40:41]
	v_lshlrev_b32_e32 v42, 16, v160
	v_and_b32_e32 v43, 0xffff0000, v160
	v_lshlrev_b32_e32 v44, 16, v161
	v_and_b32_e32 v45, 0xffff0000, v161
	v_lshlrev_b32_e32 v46, 16, v162
	v_and_b32_e32 v47, 0xffff0000, v162
	s_waitcnt lgkmcnt(0)
	v_pk_mul_f32 v[32:33], v[32:33], v[38:39] op_sel_hi:[1,0]
	v_pk_mul_f32 v[34:35], v[34:35], v[38:39] op_sel_hi:[1,0]
	v_pk_mul_f32 v[28:29], v[28:29], v[38:39] op_sel_hi:[1,0]
	v_lshl_add_u64 v[40:41], v[212:213], 1, v[40:41]
	v_lshlrev_b32_e32 v48, 16, v163
	v_and_b32_e32 v49, 0xffff0000, v163
	v_pk_fma_f32 v[34:35], v[158:159], v[34:35], v[44:45]
	v_pk_fma_f32 v[32:33], v[156:157], v[32:33], v[42:43]
	v_pk_mul_f32 v[30:31], v[30:31], v[38:39] op_sel_hi:[1,0]
	v_pk_fma_f32 v[44:45], v[152:153], v[28:29], v[46:47]
	v_cvt_pk_bf16_f32 v28, v32, v33
	v_cvt_pk_bf16_f32 v29, v34, v35
	v_pk_fma_f32 v[42:43], v[154:155], v[30:31], v[48:49]
	v_cvt_pk_bf16_f32 v30, v44, v45
	v_pk_mul_f32 v[24:25], v[24:25], v[38:39] op_sel_hi:[1,0]
	v_cvt_pk_bf16_f32 v31, v42, v43
	global_store_dwordx4 v[40:41], v[28:31], off
	v_pk_mul_f32 v[26:27], v[26:27], v[38:39] op_sel_hi:[1,0]
	v_pk_mul_f32 v[20:21], v[20:21], v[38:39] op_sel_hi:[1,0]
	v_mul_f32_e32 v28, v33, v33
	v_mul_f32_e32 v29, v35, v35
	v_fmac_f32_e32 v28, v32, v32
	v_fmac_f32_e32 v29, v34, v34
	v_add_f32_e32 v28, v28, v29
	v_mul_f32_e32 v29, v45, v45
	v_mul_f32_e32 v30, v43, v43
	v_fmac_f32_e32 v29, v44, v44
	v_fmac_f32_e32 v30, v42, v42
	v_add_f32_e32 v29, v29, v30
	v_add_f32_e32 v37, v28, v29
	v_lshlrev_b32_e32 v28, 16, v148
	v_and_b32_e32 v29, 0xffff0000, v148
	v_lshlrev_b32_e32 v30, 16, v149
	v_and_b32_e32 v31, 0xffff0000, v149
	v_lshlrev_b32_e32 v32, 16, v150
	v_and_b32_e32 v33, 0xffff0000, v150
	v_lshlrev_b32_e32 v34, 16, v151
	v_and_b32_e32 v35, 0xffff0000, v151
	v_pk_fma_f32 v[24:25], v[144:145], v[24:25], v[28:29]
	v_pk_mul_f32 v[22:23], v[22:23], v[38:39] op_sel_hi:[1,0]
	v_pk_fma_f32 v[26:27], v[146:147], v[26:27], v[30:31]
	v_pk_fma_f32 v[28:29], v[142:143], v[22:23], v[34:35]
	v_pk_fma_f32 v[22:23], v[140:141], v[20:21], v[32:33]
	v_mul_f32_e32 v21, v25, v25
	v_cvt_pk_bf16_f32 v20, v24, v25
	v_fmac_f32_e32 v21, v24, v24
	v_mul_f32_e32 v24, v27, v27
	v_fmac_f32_e32 v24, v26, v26
	v_add_f32_e32 v21, v21, v24
	v_mul_f32_e32 v24, v23, v23
	v_mul_f32_e32 v25, v29, v29
	v_fmac_f32_e32 v24, v22, v22
	v_fmac_f32_e32 v25, v28, v28
	v_add_f32_e32 v24, v24, v25
	v_add_f32_e32 v21, v21, v24
	v_add_f32_e32 v24, v37, v21
	ds_swizzle_b32 v25, v24 offset:swizzle(SWAP,16)
	v_cvt_pk_bf16_f32 v21, v26, v27
	v_cvt_pk_bf16_f32 v22, v22, v23
	v_cvt_pk_bf16_f32 v23, v28, v29
	global_store_dwordx4 v[40:41], v[20:23], off offset:256
	s_waitcnt lgkmcnt(0)
; __device__ __forceinline__ u32x4 pack8(const f32x4 a, const f32x4 b) { u32x4 w; w.x = cvt_pk_bf16(a[0], a[1]); w.y = cvt_pk_bf16(a[2], a[3]); w.z = cvt_pk_bf16(b[0], b[1]); w.w = cvt_pk_bf16(b[2], b[3]); return w; }
; __device__ __forceinline__ float bfl(unsigned w) { return __uint_as_float(w << 16); }
; __device__ __forceinline__ float bfh(unsigned w) { return __uint_as_float(w & 0xffff0000u); }
;     __device__ __forceinline__ void fused(f32x4 (&acc)[2][2][4][2], const Unit& u, int wr, int wc, int fr, int fq, PG8_LAS unsigned char* lds, int wid, int lane) const {
;     ...
;             for (int m = 0; m < 4; ++m) { const int r = ai * HALF + wr * 64 + m * 16 + fr; const float sr = S[r]; const size_t off = (size_t)(u.pm * BM + r) * DM + col0; float ss = 0.f;
; #pragma unroll
;                 for (int bj = 0; bj < 2; ++bj) { f32x4 b0, b1;
;                     if (basef) { b0 = *(const f32x4*)(basef + off + bj * HALF); b1 = *(const f32x4*)(basef + off + bj * HALF + 4); }
;                     else { const u32x4 w = pre[ai][m][bj]; b0 = (f32x4){bfl(w.x), bfh(w.x), bfl(w.y), bfh(w.y)}; b1 = (f32x4){bfl(w.z), bfh(w.z), bfl(w.w), bfh(w.w)}; }
;                     const f32x4 x0 = b0 + acc[ai][bj][m][0] * sr * gv[bj][0], x1 = b1 + acc[ai][bj][m][1] * sr * gv[bj][1];
;                     if (outf) { __builtin_nontemporal_store(x0, (f32x4*)(outf + off + bj * HALF)); __builtin_nontemporal_store(x1, (f32x4*)(outf + off + bj * HALF + 4)); }
;                     else { *(u32x4*)(xr + off + bj * HALF) = pack8(x0, x1);
;                         ss += ((x0[0] * x0[0] + x0[1] * x0[1]) + (x0[2] * x0[2] + x0[3] * x0[3])) + ((x1[0] * x1[0] + x1[1] * x1[1]) + (x1[2] * x1[2] + x1[3] * x1[3])); } }
;                 if (!outf) { ss = xor_add<16>(ss); ss = xor_add<32>(ss); if (fq == 0) P[r * 4 + wc] = ss; }
;                 if (m & 1) asm volatile("" ::: "memory"); }
;         if (outf) return;
;         asm volatile("s_waitcnt lgkmcnt(0)" ::: "memory"); __builtin_amdgcn_s_barrier(); asm volatile("" ::: "memory");
;         if (lane < 32) { const int row = wid * 32 + lane; float* rsp = (float*)(wsb + (kind == 0 ? WS_RSP_FFN : WS_RSP_MIX));
;             rsp[(size_t)(u.pm * BM + row) * 4 + u.pn] = (P[row * 4 + 0] + P[row * 4 + 1]) + (P[row * 4 + 2] + P[row * 4 + 3]); }
	s_nop 0
	v_add_f32_e32 v20, v24, v25
	v_mov_b32_e32 v21, v20
	s_nop 1
	v_permlane32_swap_b32_e32 v20, v21
	s_and_saveexec_b64 s[0:1], s[4:5]
	v_lshl_add_u32 v22, v36, 4, s20
	v_add_f32_e32 v20, v20, v21
	ds_write_b32 v22, v20
	s_or_b64 exec, exec, s[0:1]
	ds_read_b32 v22, v217 offset:8896
	v_add_u32_e32 v20, 0xb0, v214
	v_add_u32_e32 v24, v215, v20
	v_ashrrev_i32_e32 v25, 31, v24
	v_lshlrev_b64 v[24:25], 11, v[24:25]
	v_lshl_add_u64 v[24:25], s[14:15], 0, v[24:25]
	v_lshlrev_b32_e32 v26, 16, v136
	v_and_b32_e32 v27, 0xffff0000, v136
	v_lshlrev_b32_e32 v28, 16, v137
	v_and_b32_e32 v29, 0xffff0000, v137
	v_lshlrev_b32_e32 v30, 16, v138
	v_and_b32_e32 v31, 0xffff0000, v138
	s_waitcnt lgkmcnt(0)
	v_pk_mul_f32 v[16:17], v[16:17], v[22:23] op_sel_hi:[1,0]
	v_pk_mul_f32 v[18:19], v[18:19], v[22:23] op_sel_hi:[1,0]
	v_pk_mul_f32 v[12:13], v[12:13], v[22:23] op_sel_hi:[1,0]
	v_lshl_add_u64 v[24:25], v[212:213], 1, v[24:25]
	v_lshlrev_b32_e32 v32, 16, v139
	v_and_b32_e32 v33, 0xffff0000, v139
	v_pk_fma_f32 v[18:19], v[158:159], v[18:19], v[28:29]
	v_pk_fma_f32 v[16:17], v[156:157], v[16:17], v[26:27]
	v_pk_mul_f32 v[14:15], v[14:15], v[22:23] op_sel_hi:[1,0]
	v_pk_fma_f32 v[28:29], v[152:153], v[12:13], v[30:31]
	v_cvt_pk_bf16_f32 v12, v16, v17
	v_cvt_pk_bf16_f32 v13, v18, v19
	v_pk_fma_f32 v[26:27], v[154:155], v[14:15], v[32:33]
	v_cvt_pk_bf16_f32 v14, v28, v29
	v_pk_mul_f32 v[8:9], v[8:9], v[22:23] op_sel_hi:[1,0]
	v_cvt_pk_bf16_f32 v15, v26, v27
	global_store_dwordx4 v[24:25], v[12:15], off
	v_pk_mul_f32 v[10:11], v[10:11], v[22:23] op_sel_hi:[1,0]
	v_pk_mul_f32 v[4:5], v[4:5], v[22:23] op_sel_hi:[1,0]
	v_mul_f32_e32 v12, v17, v17
	v_mul_f32_e32 v13, v19, v19
	v_fmac_f32_e32 v12, v16, v16
	v_fmac_f32_e32 v13, v18, v18
	v_add_f32_e32 v12, v12, v13
	v_mul_f32_e32 v13, v29, v29
	v_mul_f32_e32 v14, v27, v27
	v_fmac_f32_e32 v13, v28, v28
	v_fmac_f32_e32 v14, v26, v26
	v_add_f32_e32 v13, v13, v14
	v_add_f32_e32 v21, v12, v13
	v_lshlrev_b32_e32 v12, 16, v132
	v_and_b32_e32 v13, 0xffff0000, v132
	v_lshlrev_b32_e32 v14, 16, v133
	v_and_b32_e32 v15, 0xffff0000, v133
	v_lshlrev_b32_e32 v16, 16, v134
	v_and_b32_e32 v17, 0xffff0000, v134
	v_lshlrev_b32_e32 v18, 16, v135
	v_and_b32_e32 v19, 0xffff0000, v135
	v_pk_fma_f32 v[8:9], v[144:145], v[8:9], v[12:13]
	v_pk_mul_f32 v[6:7], v[6:7], v[22:23] op_sel_hi:[1,0]
	v_pk_fma_f32 v[10:11], v[146:147], v[10:11], v[14:15]
	v_pk_fma_f32 v[12:13], v[142:143], v[6:7], v[18:19]
	v_pk_fma_f32 v[6:7], v[140:141], v[4:5], v[16:17]
	v_mul_f32_e32 v5, v9, v9
	v_cvt_pk_bf16_f32 v4, v8, v9
	v_fmac_f32_e32 v5, v8, v8
	v_mul_f32_e32 v8, v11, v11
	v_fmac_f32_e32 v8, v10, v10
	v_add_f32_e32 v5, v5, v8
	v_mul_f32_e32 v8, v7, v7
	v_mul_f32_e32 v9, v13, v13
	v_fmac_f32_e32 v8, v6, v6
	v_fmac_f32_e32 v9, v12, v12
	v_add_f32_e32 v8, v8, v9
	v_add_f32_e32 v5, v5, v8
	v_add_f32_e32 v8, v21, v5
	ds_swizzle_b32 v9, v8 offset:swizzle(SWAP,16)
	v_cvt_pk_bf16_f32 v5, v10, v11
	v_cvt_pk_bf16_f32 v6, v6, v7
	v_cvt_pk_bf16_f32 v7, v12, v13
	global_store_dwordx4 v[24:25], v[4:7], off offset:256
	s_waitcnt lgkmcnt(0)
	s_nop 0
	v_add_f32_e32 v4, v8, v9
	v_mov_b32_e32 v5, v4
	s_nop 1
	v_permlane32_swap_b32_e32 v4, v5
	s_and_saveexec_b64 s[0:1], s[4:5]
	v_lshl_add_u32 v6, v20, 4, s20
	v_add_f32_e32 v4, v4, v5
	ds_write_b32 v6, v4
	s_or_b64 exec, exec, s[0:1]
	s_waitcnt lgkmcnt(0)
	s_barrier
	s_and_saveexec_b64 s[0:1], s[6:7]
	s_cbranch_execz .LBB0_1357
	v_or_b32_e32 v2, v216, v2
	v_lshl_add_u32 v4, v2, 4, 0
	ds_read_b128 v[4:7], v4
	v_add_u32_e32 v8, v215, v2
	v_ashrrev_i32_e32 v9, 31, v8
	s_ashr_i32 s17, s16, 31
	s_waitcnt lgkmcnt(0)
	v_mov_b32_e32 v10, v5
	v_mov_b32_e32 v11, v6
	v_mov_b32_e32 v5, v7
	v_pk_add_f32 v[4:5], v[10:11], v[4:5]
	s_nop 0
	v_add_f32_e32 v2, v4, v5
	v_lshl_add_u64 v[4:5], v[8:9], 4, s[12:13]
	v_lshl_add_u64 v[4:5], s[16:17], 2, v[4:5]
	v_add_co_u32_e32 v4, vcc, 0x640000, v4
	s_nop 1
	v_addc_co_u32_e32 v5, vcc, 0, v5, vcc
	global_store_dword v[4:5], v2, off

;     __device__ __forceinline__ void fused(f32x4 (&acc)[2][2][4][2], const Unit& u, int wr, int wc, int fr, int fq, PG8_LAS unsigned char* lds, int wid, int lane) const {
;     ...
;         if (!basef) {
; #pragma unroll
;             for (int ai = 0; ai < 2; ++ai)
; #pragma unroll
;             for (int m = 0; m < 4; ++m) { const size_t off = (size_t)(u.pm * BM + ai * HALF + wr * 64 + m * 16 + fr) * DM + col0;
; #pragma unroll
;                 for (int bj = 0; bj < 2; ++bj) pre[ai][m][bj] = *(const u32x4*)(xr + off + bj * HALF); }
;     ...
;         f32x4 gv[2][2];
; #pragma unroll
;         for (int bj = 0; bj < 2; ++bj)
; #pragma unroll
;             for (int n = 0; n < 2; ++n) gv[bj][n] = *(const f32x4*)(g1 + col0 + bj * HALF + 4 * n);
.LBB0_1807:
	s_or_b64 exec, exec, s[8:9]
	s_lshl_b32 s8, s25, 5
	s_lshl_b32 s9, s16, 8
	v_lshrrev_b32_e32 v132, 1, v146
	s_or_b32 s8, s9, s8
	v_and_or_b32 v214, v132, 24, s8
	v_add_u32_e32 v132, s24, v229
	v_or_b32_e32 v132, v132, v147
	v_ashrrev_i32_e32 v215, 31, v214
	v_lshl_add_u64 v[134:135], v[214:215], 1, s[12:13]
	s_mov_b64 s[8:9], 0x14000000
	v_ashrrev_i32_e32 v133, 31, v132
	v_lshl_add_u64 v[212:213], v[134:135], 0, s[8:9]
	v_lshlrev_b64 v[134:135], 11, v[132:133]
	v_lshl_add_u64 v[134:135], v[212:213], 0, v[134:135]
	global_load_dwordx4 v[208:211], v[134:135], off
	global_load_dwordx4 v[204:207], v[134:135], off offset:256
	v_or_b32_e32 v134, 16, v132
	v_ashrrev_i32_e32 v135, 31, v134
	v_lshlrev_b64 v[134:135], 11, v[134:135]
	v_lshl_add_u64 v[134:135], v[212:213], 0, v[134:135]
	global_load_dwordx4 v[200:203], v[134:135], off
	global_load_dwordx4 v[196:199], v[134:135], off offset:256
	v_or_b32_e32 v134, 32, v132
	v_ashrrev_i32_e32 v135, 31, v134
	v_lshlrev_b64 v[134:135], 11, v[134:135]
	v_lshl_add_u64 v[134:135], v[212:213], 0, v[134:135]
	global_load_dwordx4 v[192:195], v[134:135], off
	global_load_dwordx4 v[188:191], v[134:135], off offset:256
	v_or_b32_e32 v134, 48, v132
	v_ashrrev_i32_e32 v135, 31, v134
	v_lshlrev_b64 v[134:135], 11, v[134:135]
	v_lshl_add_u64 v[134:135], v[212:213], 0, v[134:135]
	global_load_dwordx4 v[184:187], v[134:135], off
	global_load_dwordx4 v[180:183], v[134:135], off offset:256
	v_add_u32_e32 v134, 0x80, v132
	v_ashrrev_i32_e32 v135, 31, v134
	v_lshlrev_b64 v[134:135], 11, v[134:135]
	v_lshl_add_u64 v[134:135], v[212:213], 0, v[134:135]
	global_load_dwordx4 v[176:179], v[134:135], off
	global_load_dwordx4 v[172:175], v[134:135], off offset:256
	v_add_u32_e32 v134, 0x90, v132
	v_ashrrev_i32_e32 v135, 31, v134
	v_lshlrev_b64 v[134:135], 11, v[134:135]
	v_lshl_add_u64 v[134:135], v[212:213], 0, v[134:135]
	global_load_dwordx4 v[168:171], v[134:135], off
	global_load_dwordx4 v[164:167], v[134:135], off offset:256
	v_add_u32_e32 v134, 0xa0, v132
	v_add_u32_e32 v132, 0xb0, v132
	v_ashrrev_i32_e32 v135, 31, v134
	v_ashrrev_i32_e32 v133, 31, v132
	v_lshlrev_b64 v[134:135], 11, v[134:135]
	v_lshlrev_b64 v[132:133], 11, v[132:133]
	v_lshl_add_u64 v[134:135], v[212:213], 0, v[134:135]
	v_lshl_add_u64 v[132:133], v[212:213], 0, v[132:133]
	global_load_dwordx4 v[160:163], v[134:135], off
	global_load_dwordx4 v[152:155], v[134:135], off offset:256
	global_load_dwordx4 v[136:139], v[132:133], off
	s_nop 0
	global_load_dwordx4 v[132:135], v[132:133], off offset:256
	s_memrealtime s[14:15]
	v_and_or_b32 v146, v146, 31, v230
	v_add_u32_e32 v140, v229, v146
	v_ashrrev_i32_e32 v141, 31, v140
	v_lshl_add_u64 v[144:145], v[140:141], 4, s[0:1]
	s_lshl_b32 s36, s77, 10
	s_lshl_b64 s[0:1], s[36:37], 2
	s_add_u32 s0, s12, s0
	s_addc_u32 s1, s13, s1
	v_lshl_add_u64 v[252:253], v[214:215], 2, s[0:1]
	s_mov_b64 s[0:1], 0x714000
	v_lshl_add_u64 v[252:253], v[252:253], 0, s[0:1]
	global_load_dwordx4 v[236:239], v[252:253], off
	global_load_dwordx4 v[240:243], v[252:253], off offset:16
	global_load_dwordx4 v[244:247], v[252:253], off offset:512
	global_load_dwordx4 v[248:251], v[252:253], off offset:528
	s_branch .LBB0_1809

; __device__ __forceinline__ u32x4 pack8(const f32x4 a, const f32x4 b) { u32x4 w; w.x = cvt_pk_bf16(a[0], a[1]); w.y = cvt_pk_bf16(a[2], a[3]); w.z = cvt_pk_bf16(b[0], b[1]); w.w = cvt_pk_bf16(b[2], b[3]); return w; }
; __device__ __forceinline__ float bfl(unsigned w) { return __uint_as_float(w << 16); }
; __device__ __forceinline__ float bfh(unsigned w) { return __uint_as_float(w & 0xffff0000u); }
;     __device__ __forceinline__ void fused(f32x4 (&acc)[2][2][4][2], const Unit& u, int wr, int wc, int fr, int fq, PG8_LAS unsigned char* lds, int wid, int lane) const {
;     ...
;         f32x4 gv[2][2];
; #pragma unroll
;         for (int bj = 0; bj < 2; ++bj)
; #pragma unroll
;             for (int n = 0; n < 2; ++n) gv[bj][n] = *(const f32x4*)(g1 + col0 + bj * HALF + 4 * n);
; #pragma unroll
;         for (int ai = 0; ai < 2; ++ai)
; #pragma unroll
;             for (int m = 0; m < 4; ++m) { const int r = ai * HALF + wr * 64 + m * 16 + fr; const float sr = S[r]; const size_t off = (size_t)(u.pm * BM + r) * DM + col0; float ss = 0.f;
; #pragma unroll
;                 for (int bj = 0; bj < 2; ++bj) { f32x4 b0, b1;
;                     if (basef) { b0 = *(const f32x4*)(basef + off + bj * HALF); b1 = *(const f32x4*)(basef + off + bj * HALF + 4); }
;                     else { const u32x4 w = pre[ai][m][bj]; b0 = (f32x4){bfl(w.x), bfh(w.x), bfl(w.y), bfh(w.y)}; b1 = (f32x4){bfl(w.z), bfh(w.z), bfl(w.w), bfh(w.w)}; }
;                     const f32x4 x0 = b0 + acc[ai][bj][m][0] * sr * gv[bj][0], x1 = b1 + acc[ai][bj][m][1] * sr * gv[bj][1];
;                     if (outf) { __builtin_nontemporal_store(x0, (f32x4*)(outf + off + bj * HALF)); __builtin_nontemporal_store(x1, (f32x4*)(outf + off + bj * HALF + 4)); }
;                     else { *(u32x4*)(xr + off + bj * HALF) = pack8(x0, x1);
;                         ss += ((x0[0] * x0[0] + x0[1] * x0[1]) + (x0[2] * x0[2] + x0[3] * x0[3])) + ((x1[0] * x1[0] + x1[1] * x1[1]) + (x1[2] * x1[2] + x1[3] * x1[3])); } }
;                 if (!outf) { ss = xor_add<16>(ss); ss = xor_add<32>(ss); if (fq == 0) P[r * 4 + wc] = ss; }
.LBB0_1819:
	s_or_b64 exec, exec, s[0:1]
	s_lshl_b32 s36, s77, 10
	s_lshl_b64 s[0:1], s[36:37], 2
	s_add_u32 s0, s12, s0
	s_addc_u32 s1, s13, s1
	v_lshl_add_u64 v[140:141], v[214:215], 2, s[0:1]
	s_mov_b64 s[0:1], 0x714000
	s_waitcnt lgkmcnt(0)
	s_barrier
	v_lshl_add_u64 v[142:143], v[140:141], 0, s[0:1]
	s_mov_b32 s0, 0x714000
	v_add_co_u32_e32 v140, vcc, s0, v140
	v_mov_b32_e32 v148, v240
	v_mov_b32_e32 v149, v241
	v_mov_b32_e32 v150, v242
	v_mov_b32_e32 v151, v243
	s_nop 0
	v_addc_co_u32_e32 v141, vcc, 0, v141, vcc
	v_mov_b32_e32 v156, v236
	v_mov_b32_e32 v157, v237
	v_mov_b32_e32 v158, v238
	v_mov_b32_e32 v159, v239
	v_mov_b32_e32 v144, v244
	v_mov_b32_e32 v145, v245
	v_mov_b32_e32 v146, v246
	v_mov_b32_e32 v147, v247
	s_nop 0
	v_mov_b32_e32 v140, v248
	v_mov_b32_e32 v141, v249
	v_mov_b32_e32 v142, v250
	v_mov_b32_e32 v143, v251
	v_lshl_add_u32 v231, v228, 2, 0
	ds_read_b32 v216, v231 offset:8192
	v_readlane_b32 s0, v255, 15
	v_add_u32_e32 v218, v229, v228
	s_cmp_eq_u32 s77, 3
	v_readlane_b32 s1, v255, 16
	v_ashrrev_i32_e32 v219, 31, v218
	s_waitcnt lgkmcnt(0)
	s_cselect_b32 s15, s1, 0
	s_cselect_b32 s14, s0, 0
	s_waitcnt vmcnt(0)
	v_lshlrev_b32_e32 v232, 16, v210
	v_and_b32_e32 v233, 0xffff0000, v210
	v_lshlrev_b32_e32 v234, 16, v211
	v_and_b32_e32 v235, 0xffff0000, v211
	v_lshlrev_b64 v[210:211], 10, v[218:219]
	s_cmp_eq_u64 s[14:15], 0
	v_lshlrev_b32_e32 v220, 16, v208
	v_and_b32_e32 v221, 0xffff0000, v208
	v_lshlrev_b32_e32 v208, 16, v209
	v_and_b32_e32 v209, 0xffff0000, v209
	v_lshl_add_u64 v[210:211], v[210:211], 0, v[214:215]
	v_pk_mul_f32 v[130:131], v[130:131], v[216:217] op_sel_hi:[1,0]
	v_pk_mul_f32 v[128:129], v[128:129], v[216:217] op_sel_hi:[1,0]
	v_pk_mul_f32 v[124:125], v[124:125], v[216:217] op_sel_hi:[1,0]
	v_pk_mul_f32 v[126:127], v[126:127], v[216:217] op_sel_hi:[1,0]
	s_cselect_b64 s[0:1], -1, 0
	s_cmp_lg_u64 s[14:15], 0
	s_mov_b64 s[10:11], -1
	v_lshl_add_u64 v[210:211], v[210:211], 2, s[14:15]
	s_cselect_b64 s[8:9], -1, 0
	s_and_b64 vcc, exec, s[0:1]
	v_pk_fma_f32 v[126:127], v[150:151], v[126:127], v[234:235]
	v_pk_fma_f32 v[124:125], v[148:149], v[124:125], v[232:233]
	v_pk_fma_f32 v[128:129], v[156:157], v[128:129], v[220:221]
	v_pk_fma_f32 v[130:131], v[158:159], v[130:131], v[208:209]
	s_cbranch_vccnz .LBB0_1821
	s_mov_b64 s[10:11], 0
	global_store_dwordx4 v[210:211], v[128:131], off nt
	global_store_dwordx4 v[210:211], v[124:127], off offset:16 nt
